# combo8 + P4 epilogue end: dword touch-loads of the next unit's residual tile lines into a phase-unused VGPR (cache warm-up during the next main loop)
# baseline (speedup 1.0000x reference)
.LBB0_565:
	s_andn2_b64 vcc, exec, s[4:5]
	s_mov_b64 s[4:5], -1
	s_ashr_i32 s21, s28, 4
	s_mul_hi_i32 s23, s21, 0x18000
	s_mul_i32 s21, s21, 0x18000
	s_add_u32 s30, s45, s21
	s_addc_u32 s31, s46, s23
	v_lshl_or_b32 v224, s54, 8, v197
	v_mov_b32_e32 v225, 0
	v_lshl_add_u64 v[226:227], v[224:225], 2, s[30:31]
	global_load_dwordx4 v[200:203], v[226:227], off
	global_load_dwordx4 v[204:207], v[226:227], off offset:64
	global_load_dwordx4 v[208:211], v[226:227], off offset:512
	global_load_dwordx4 v[212:215], v[226:227], off offset:576
	v_lshl_add_u32 v228, s28, 8, v180
	v_mov_b32_e32 v229, 0
	v_lshlrev_b64 v[216:217], 14, v[228:229]
	v_lshl_add_u64 v[216:217], v[216:217], 0, s[8:9]
	v_lshl_add_u64 v[216:217], v[224:225], 2, v[216:217]
	v_lshlrev_b64 v[218:219], 13, v[228:229]
	v_lshl_add_u64 v[218:219], v[218:219], 0, s[12:13]
	v_and_b32_e32 v230, 12, v197
	v_add_u32_e32 v230, v230, v224
	v_mov_b32_e32 v231, 0
	v_lshl_add_u64 v[218:219], v[230:231], 1, v[218:219]
	s_mov_b32 s30, 0x0
	s_mov_b32 s31, 0
	v_lshl_add_u64 v[220:221], v[216:217], 0, s[30:31]
	global_load_dwordx4 v[0:3], v[220:221], off
	global_load_dwordx4 v[4:7], v[220:221], off offset:64
	s_mov_b32 s30, 0x0
	s_mov_b32 s31, 0
	v_lshl_add_u64 v[220:221], v[216:217], 0, s[30:31]
	global_load_dwordx4 v[8:11], v[220:221], off offset:512
	global_load_dwordx4 v[12:15], v[220:221], off offset:576
	s_mov_b32 s30, 0x40000
	s_mov_b32 s31, 0
	v_lshl_add_u64 v[220:221], v[216:217], 0, s[30:31]
	global_load_dwordx4 v[16:19], v[220:221], off
	global_load_dwordx4 v[20:23], v[220:221], off offset:64
	s_mov_b32 s30, 0x40000
	s_mov_b32 s31, 0
	v_lshl_add_u64 v[220:221], v[216:217], 0, s[30:31]
	global_load_dwordx4 v[24:27], v[220:221], off offset:512
	global_load_dwordx4 v[28:31], v[220:221], off offset:576
	s_mov_b32 s30, 0x80000
	s_mov_b32 s31, 0
	v_lshl_add_u64 v[220:221], v[216:217], 0, s[30:31]
	global_load_dwordx4 v[172:175], v[220:221], off
	global_load_dwordx4 v[176:179], v[220:221], off offset:64
	s_waitcnt vmcnt(10)
	v_mul_f32_e32 v200, s18, v200
	v_mul_f32_e32 v201, s18, v201
	v_mul_f32_e32 v202, s18, v202
	v_mul_f32_e32 v203, s18, v203
	v_mul_f32_e32 v204, s18, v204
	v_mul_f32_e32 v205, s18, v205
	v_mul_f32_e32 v206, s18, v206
	v_mul_f32_e32 v207, s18, v207
	v_mul_f32_e32 v208, s18, v208
	v_mul_f32_e32 v209, s18, v209
	v_mul_f32_e32 v210, s18, v210
	v_mul_f32_e32 v211, s18, v211
	v_mul_f32_e32 v212, s18, v212
	v_mul_f32_e32 v213, s18, v213
	v_mul_f32_e32 v214, s18, v214
	v_mul_f32_e32 v215, s18, v215
	s_waitcnt vmcnt(8)
	v_fma_f32 v0, v156, v200, v0
	v_fma_f32 v1, v157, v201, v1
	v_fma_f32 v2, v158, v202, v2
	v_fma_f32 v3, v159, v203, v3
	v_fma_f32 v4, v152, v204, v4
	v_fma_f32 v5, v153, v205, v5
	v_fma_f32 v6, v154, v206, v6
	v_fma_f32 v7, v155, v207, v7
	v_cvt_pk_bf16_f32 v0, v0, v1
	v_cvt_pk_bf16_f32 v1, v2, v3
	v_cvt_pk_bf16_f32 v2, v4, v5
	v_cvt_pk_bf16_f32 v3, v6, v7
	s_mov_b32 s30, 0x0
	s_mov_b32 s31, 0
	v_lshl_add_u64 v[222:223], v[218:219], 0, s[30:31]
	s_nop 1
	v_permlane32_swap_b32_e32 v0, v2
	v_permlane32_swap_b32_e32 v1, v3
	s_nop 1
	v_permlane16_swap_b32_e32 v0, v2
	v_permlane16_swap_b32_e32 v1, v3
	global_store_dwordx4 v[222:223], v[0:3], off
	s_mov_b32 s30, 0x80000
	s_mov_b32 s31, 0
	v_lshl_add_u64 v[220:221], v[216:217], 0, s[30:31]
	global_load_dwordx4 v[0:3], v[220:221], off offset:512
	global_load_dwordx4 v[4:7], v[220:221], off offset:576
	s_waitcnt vmcnt(9)
	v_fma_f32 v8, v140, v208, v8
	v_fma_f32 v9, v141, v209, v9
	v_fma_f32 v10, v142, v210, v10
	v_fma_f32 v11, v143, v211, v11
	v_fma_f32 v12, v136, v212, v12
	v_fma_f32 v13, v137, v213, v13
	v_fma_f32 v14, v138, v214, v14
	v_fma_f32 v15, v139, v215, v15
	v_cvt_pk_bf16_f32 v8, v8, v9
	v_cvt_pk_bf16_f32 v9, v10, v11
	v_cvt_pk_bf16_f32 v10, v12, v13
	v_cvt_pk_bf16_f32 v11, v14, v15
	s_mov_b32 s30, 0x0
	s_mov_b32 s31, 0
	v_lshl_add_u64 v[222:223], v[218:219], 0, s[30:31]
	s_nop 1
	v_permlane32_swap_b32_e32 v8, v10
	v_permlane32_swap_b32_e32 v9, v11
	s_nop 1
	v_permlane16_swap_b32_e32 v8, v10
	v_permlane16_swap_b32_e32 v9, v11
	global_store_dwordx4 v[222:223], v[8:11], off offset:256
	s_mov_b32 s30, 0xc0000
	s_mov_b32 s31, 0
	v_lshl_add_u64 v[220:221], v[216:217], 0, s[30:31]
	global_load_dwordx4 v[8:11], v[220:221], off
	global_load_dwordx4 v[12:15], v[220:221], off offset:64
	s_waitcnt vmcnt(10)
	v_fma_f32 v16, v148, v200, v16
	v_fma_f32 v17, v149, v201, v17
	v_fma_f32 v18, v150, v202, v18
	v_fma_f32 v19, v151, v203, v19
	v_fma_f32 v20, v144, v204, v20
	v_fma_f32 v21, v145, v205, v21
	v_fma_f32 v22, v146, v206, v22
	v_fma_f32 v23, v147, v207, v23
	v_cvt_pk_bf16_f32 v16, v16, v17
	v_cvt_pk_bf16_f32 v17, v18, v19
	v_cvt_pk_bf16_f32 v18, v20, v21
	v_cvt_pk_bf16_f32 v19, v22, v23
	s_mov_b32 s30, 0x20000
	s_mov_b32 s31, 0
	v_lshl_add_u64 v[222:223], v[218:219], 0, s[30:31]
	s_nop 1
	v_permlane32_swap_b32_e32 v16, v18
	v_permlane32_swap_b32_e32 v17, v19
	s_nop 1
	v_permlane16_swap_b32_e32 v16, v18
	v_permlane16_swap_b32_e32 v17, v19
	global_store_dwordx4 v[222:223], v[16:19], off
	s_mov_b32 s30, 0xc0000
	s_mov_b32 s31, 0
	v_lshl_add_u64 v[220:221], v[216:217], 0, s[30:31]
	global_load_dwordx4 v[16:19], v[220:221], off offset:512
	global_load_dwordx4 v[20:23], v[220:221], off offset:576
	s_waitcnt vmcnt(11)
	v_fma_f32 v24, v132, v208, v24
	v_fma_f32 v25, v133, v209, v25
	v_fma_f32 v26, v134, v210, v26
	v_fma_f32 v27, v135, v211, v27
	v_fma_f32 v28, v128, v212, v28
	v_fma_f32 v29, v129, v213, v29
	v_fma_f32 v30, v130, v214, v30
	v_fma_f32 v31, v131, v215, v31
	v_cvt_pk_bf16_f32 v24, v24, v25
	v_cvt_pk_bf16_f32 v25, v26, v27
	v_cvt_pk_bf16_f32 v26, v28, v29
	v_cvt_pk_bf16_f32 v27, v30, v31
	s_mov_b32 s30, 0x20000
	s_mov_b32 s31, 0
	v_lshl_add_u64 v[222:223], v[218:219], 0, s[30:31]
	s_nop 1
	v_permlane32_swap_b32_e32 v24, v26
	v_permlane32_swap_b32_e32 v25, v27
	s_nop 1
	v_permlane16_swap_b32_e32 v24, v26
	v_permlane16_swap_b32_e32 v25, v27
	global_store_dwordx4 v[222:223], v[24:27], off offset:256
	s_mov_b32 s30, 0x200000
	s_mov_b32 s31, 0
	v_lshl_add_u64 v[220:221], v[216:217], 0, s[30:31]
	global_load_dwordx4 v[24:27], v[220:221], off
	global_load_dwordx4 v[28:31], v[220:221], off offset:64
	s_waitcnt vmcnt(12)
	v_fma_f32 v172, v124, v200, v172
	v_fma_f32 v173, v125, v201, v173
	v_fma_f32 v174, v126, v202, v174
	v_fma_f32 v175, v127, v203, v175
	v_fma_f32 v176, v120, v204, v176
	v_fma_f32 v177, v121, v205, v177
	v_fma_f32 v178, v122, v206, v178
	v_fma_f32 v179, v123, v207, v179
	v_cvt_pk_bf16_f32 v172, v172, v173
	v_cvt_pk_bf16_f32 v173, v174, v175
	v_cvt_pk_bf16_f32 v174, v176, v177
	v_cvt_pk_bf16_f32 v175, v178, v179
	s_mov_b32 s30, 0x40000
	s_mov_b32 s31, 0
	v_lshl_add_u64 v[222:223], v[218:219], 0, s[30:31]
	s_nop 1
	v_permlane32_swap_b32_e32 v172, v174
	v_permlane32_swap_b32_e32 v173, v175
	s_nop 1
	v_permlane16_swap_b32_e32 v172, v174
	v_permlane16_swap_b32_e32 v173, v175
	global_store_dwordx4 v[222:223], v[172:175], off
	s_mov_b32 s30, 0x200000
	s_mov_b32 s31, 0
	v_lshl_add_u64 v[220:221], v[216:217], 0, s[30:31]
	global_load_dwordx4 v[172:175], v[220:221], off offset:512
	global_load_dwordx4 v[176:179], v[220:221], off offset:576
	s_waitcnt vmcnt(12)
	v_fma_f32 v0, v108, v208, v0
	v_fma_f32 v1, v109, v209, v1
	v_fma_f32 v2, v110, v210, v2
	v_fma_f32 v3, v111, v211, v3
	v_fma_f32 v4, v104, v212, v4
	v_fma_f32 v5, v105, v213, v5
	v_fma_f32 v6, v106, v214, v6
	v_fma_f32 v7, v107, v215, v7
	v_cvt_pk_bf16_f32 v0, v0, v1
	v_cvt_pk_bf16_f32 v1, v2, v3
	v_cvt_pk_bf16_f32 v2, v4, v5
	v_cvt_pk_bf16_f32 v3, v6, v7
	s_mov_b32 s30, 0x40000
	s_mov_b32 s31, 0
	v_lshl_add_u64 v[222:223], v[218:219], 0, s[30:31]
	s_nop 1
	v_permlane32_swap_b32_e32 v0, v2
	v_permlane32_swap_b32_e32 v1, v3
	s_nop 1
	v_permlane16_swap_b32_e32 v0, v2
	v_permlane16_swap_b32_e32 v1, v3
	global_store_dwordx4 v[222:223], v[0:3], off offset:256
	s_mov_b32 s30, 0x240000
	s_mov_b32 s31, 0
	v_lshl_add_u64 v[220:221], v[216:217], 0, s[30:31]
	global_load_dwordx4 v[0:3], v[220:221], off
	global_load_dwordx4 v[4:7], v[220:221], off offset:64
	s_waitcnt vmcnt(12)
	v_fma_f32 v8, v116, v200, v8
	v_fma_f32 v9, v117, v201, v9
	v_fma_f32 v10, v118, v202, v10
	v_fma_f32 v11, v119, v203, v11
	v_fma_f32 v12, v112, v204, v12
	v_fma_f32 v13, v113, v205, v13
	v_fma_f32 v14, v114, v206, v14
	v_fma_f32 v15, v115, v207, v15
	v_cvt_pk_bf16_f32 v8, v8, v9
	v_cvt_pk_bf16_f32 v9, v10, v11
	v_cvt_pk_bf16_f32 v10, v12, v13
	v_cvt_pk_bf16_f32 v11, v14, v15
	s_mov_b32 s30, 0x60000
	s_mov_b32 s31, 0
	v_lshl_add_u64 v[222:223], v[218:219], 0, s[30:31]
	s_nop 1
	v_permlane32_swap_b32_e32 v8, v10
	v_permlane32_swap_b32_e32 v9, v11
	s_nop 1
	v_permlane16_swap_b32_e32 v8, v10
	v_permlane16_swap_b32_e32 v9, v11
	global_store_dwordx4 v[222:223], v[8:11], off
	s_mov_b32 s30, 0x240000
	s_mov_b32 s31, 0
	v_lshl_add_u64 v[220:221], v[216:217], 0, s[30:31]
	global_load_dwordx4 v[8:11], v[220:221], off offset:512
	global_load_dwordx4 v[12:15], v[220:221], off offset:576
	s_waitcnt vmcnt(12)
	v_fma_f32 v16, v100, v208, v16
	v_fma_f32 v17, v101, v209, v17
	v_fma_f32 v18, v102, v210, v18
	v_fma_f32 v19, v103, v211, v19
	v_fma_f32 v20, v96, v212, v20
	v_fma_f32 v21, v97, v213, v21
	v_fma_f32 v22, v98, v214, v22
	v_fma_f32 v23, v99, v215, v23
	v_cvt_pk_bf16_f32 v16, v16, v17
	v_cvt_pk_bf16_f32 v17, v18, v19
	v_cvt_pk_bf16_f32 v18, v20, v21
	v_cvt_pk_bf16_f32 v19, v22, v23
	s_mov_b32 s30, 0x60000
	s_mov_b32 s31, 0
	v_lshl_add_u64 v[222:223], v[218:219], 0, s[30:31]
	s_nop 1
	v_permlane32_swap_b32_e32 v16, v18
	v_permlane32_swap_b32_e32 v17, v19
	s_nop 1
	v_permlane16_swap_b32_e32 v16, v18
	v_permlane16_swap_b32_e32 v17, v19
	global_store_dwordx4 v[222:223], v[16:19], off offset:256
	s_mov_b32 s30, 0x280000
	s_mov_b32 s31, 0
	v_lshl_add_u64 v[220:221], v[216:217], 0, s[30:31]
	global_load_dwordx4 v[16:19], v[220:221], off
	global_load_dwordx4 v[20:23], v[220:221], off offset:64
	s_waitcnt vmcnt(12)
	v_fma_f32 v24, v92, v200, v24
	v_fma_f32 v25, v93, v201, v25
	v_fma_f32 v26, v94, v202, v26
	v_fma_f32 v27, v95, v203, v27
	v_fma_f32 v28, v88, v204, v28
	v_fma_f32 v29, v89, v205, v29
	v_fma_f32 v30, v90, v206, v30
	v_fma_f32 v31, v91, v207, v31
	v_cvt_pk_bf16_f32 v24, v24, v25
	v_cvt_pk_bf16_f32 v25, v26, v27
	v_cvt_pk_bf16_f32 v26, v28, v29
	v_cvt_pk_bf16_f32 v27, v30, v31
	s_mov_b32 s30, 0x100000
	s_mov_b32 s31, 0
	v_lshl_add_u64 v[222:223], v[218:219], 0, s[30:31]
	s_nop 1
	v_permlane32_swap_b32_e32 v24, v26
	v_permlane32_swap_b32_e32 v25, v27
	s_nop 1
	v_permlane16_swap_b32_e32 v24, v26
	v_permlane16_swap_b32_e32 v25, v27
	global_store_dwordx4 v[222:223], v[24:27], off
	s_mov_b32 s30, 0x280000
	s_mov_b32 s31, 0
	v_lshl_add_u64 v[220:221], v[216:217], 0, s[30:31]
	global_load_dwordx4 v[24:27], v[220:221], off offset:512
	global_load_dwordx4 v[28:31], v[220:221], off offset:576
	s_waitcnt vmcnt(12)
	v_fma_f32 v172, v76, v208, v172
	v_fma_f32 v173, v77, v209, v173
	v_fma_f32 v174, v78, v210, v174
	v_fma_f32 v175, v79, v211, v175
	v_fma_f32 v176, v72, v212, v176
	v_fma_f32 v177, v73, v213, v177
	v_fma_f32 v178, v74, v214, v178
	v_fma_f32 v179, v75, v215, v179
	v_cvt_pk_bf16_f32 v172, v172, v173
	v_cvt_pk_bf16_f32 v173, v174, v175
	v_cvt_pk_bf16_f32 v174, v176, v177
	v_cvt_pk_bf16_f32 v175, v178, v179
	s_mov_b32 s30, 0x100000
	s_mov_b32 s31, 0
	v_lshl_add_u64 v[222:223], v[218:219], 0, s[30:31]
	s_nop 1
	v_permlane32_swap_b32_e32 v172, v174
	v_permlane32_swap_b32_e32 v173, v175
	s_nop 1
	v_permlane16_swap_b32_e32 v172, v174
	v_permlane16_swap_b32_e32 v173, v175
	global_store_dwordx4 v[222:223], v[172:175], off offset:256
	s_mov_b32 s30, 0x2c0000
	s_mov_b32 s31, 0
	v_lshl_add_u64 v[220:221], v[216:217], 0, s[30:31]
	global_load_dwordx4 v[172:175], v[220:221], off
	global_load_dwordx4 v[176:179], v[220:221], off offset:64
	s_waitcnt vmcnt(12)
	v_fma_f32 v0, v84, v200, v0
	v_fma_f32 v1, v85, v201, v1
	v_fma_f32 v2, v86, v202, v2
	v_fma_f32 v3, v87, v203, v3
	v_fma_f32 v4, v80, v204, v4
	v_fma_f32 v5, v81, v205, v5
	v_fma_f32 v6, v82, v206, v6
	v_fma_f32 v7, v83, v207, v7
	v_cvt_pk_bf16_f32 v0, v0, v1
	v_cvt_pk_bf16_f32 v1, v2, v3
	v_cvt_pk_bf16_f32 v2, v4, v5
	v_cvt_pk_bf16_f32 v3, v6, v7
	s_mov_b32 s30, 0x120000
	s_mov_b32 s31, 0
	v_lshl_add_u64 v[222:223], v[218:219], 0, s[30:31]
	s_nop 1
	v_permlane32_swap_b32_e32 v0, v2
	v_permlane32_swap_b32_e32 v1, v3
	s_nop 1
	v_permlane16_swap_b32_e32 v0, v2
	v_permlane16_swap_b32_e32 v1, v3
	global_store_dwordx4 v[222:223], v[0:3], off
	s_mov_b32 s30, 0x2c0000
	s_mov_b32 s31, 0
	v_lshl_add_u64 v[220:221], v[216:217], 0, s[30:31]
	global_load_dwordx4 v[0:3], v[220:221], off offset:512
	global_load_dwordx4 v[4:7], v[220:221], off offset:576
	s_waitcnt vmcnt(12)
	v_fma_f32 v8, v68, v208, v8
	v_fma_f32 v9, v69, v209, v9
	v_fma_f32 v10, v70, v210, v10
	v_fma_f32 v11, v71, v211, v11
	v_fma_f32 v12, v64, v212, v12
	v_fma_f32 v13, v65, v213, v13
	v_fma_f32 v14, v66, v214, v14
	v_fma_f32 v15, v67, v215, v15
	v_cvt_pk_bf16_f32 v8, v8, v9
	v_cvt_pk_bf16_f32 v9, v10, v11
	v_cvt_pk_bf16_f32 v10, v12, v13
	v_cvt_pk_bf16_f32 v11, v14, v15
	s_mov_b32 s30, 0x120000
	s_mov_b32 s31, 0
	v_lshl_add_u64 v[222:223], v[218:219], 0, s[30:31]
	s_nop 1
	v_permlane32_swap_b32_e32 v8, v10
	v_permlane32_swap_b32_e32 v9, v11
	s_nop 1
	v_permlane16_swap_b32_e32 v8, v10
	v_permlane16_swap_b32_e32 v9, v11
	global_store_dwordx4 v[222:223], v[8:11], off offset:256
	s_waitcnt vmcnt(10)
	v_fma_f32 v16, v60, v200, v16
	v_fma_f32 v17, v61, v201, v17
	v_fma_f32 v18, v62, v202, v18
	v_fma_f32 v19, v63, v203, v19
	v_fma_f32 v20, v56, v204, v20
	v_fma_f32 v21, v57, v205, v21
	v_fma_f32 v22, v58, v206, v22
	v_fma_f32 v23, v59, v207, v23
	v_cvt_pk_bf16_f32 v16, v16, v17
	v_cvt_pk_bf16_f32 v17, v18, v19
	v_cvt_pk_bf16_f32 v18, v20, v21
	v_cvt_pk_bf16_f32 v19, v22, v23
	s_mov_b32 s30, 0x140000
	s_mov_b32 s31, 0
	v_lshl_add_u64 v[222:223], v[218:219], 0, s[30:31]
	s_nop 1
	v_permlane32_swap_b32_e32 v16, v18
	v_permlane32_swap_b32_e32 v17, v19
	s_nop 1
	v_permlane16_swap_b32_e32 v16, v18
	v_permlane16_swap_b32_e32 v17, v19
	global_store_dwordx4 v[222:223], v[16:19], off
	s_waitcnt vmcnt(8)
	v_fma_f32 v24, v44, v208, v24
	v_fma_f32 v25, v45, v209, v25
	v_fma_f32 v26, v46, v210, v26
	v_fma_f32 v27, v47, v211, v27
	v_fma_f32 v28, v40, v212, v28
	v_fma_f32 v29, v41, v213, v29
	v_fma_f32 v30, v42, v214, v30
	v_fma_f32 v31, v43, v215, v31
	v_cvt_pk_bf16_f32 v24, v24, v25
	v_cvt_pk_bf16_f32 v25, v26, v27
	v_cvt_pk_bf16_f32 v26, v28, v29
	v_cvt_pk_bf16_f32 v27, v30, v31
	s_mov_b32 s30, 0x140000
	s_mov_b32 s31, 0
	v_lshl_add_u64 v[222:223], v[218:219], 0, s[30:31]
	s_nop 1
	v_permlane32_swap_b32_e32 v24, v26
	v_permlane32_swap_b32_e32 v25, v27
	s_nop 1
	v_permlane16_swap_b32_e32 v24, v26
	v_permlane16_swap_b32_e32 v25, v27
	global_store_dwordx4 v[222:223], v[24:27], off offset:256
	s_waitcnt vmcnt(6)
	v_fma_f32 v172, v52, v200, v172
	v_fma_f32 v173, v53, v201, v173
	v_fma_f32 v174, v54, v202, v174
	v_fma_f32 v175, v55, v203, v175
	v_fma_f32 v176, v48, v204, v176
	v_fma_f32 v177, v49, v205, v177
	v_fma_f32 v178, v50, v206, v178
	v_fma_f32 v179, v51, v207, v179
	v_cvt_pk_bf16_f32 v172, v172, v173
	v_cvt_pk_bf16_f32 v173, v174, v175
	v_cvt_pk_bf16_f32 v174, v176, v177
	v_cvt_pk_bf16_f32 v175, v178, v179
	s_mov_b32 s30, 0x160000
	s_mov_b32 s31, 0
	v_lshl_add_u64 v[222:223], v[218:219], 0, s[30:31]
	s_nop 1
	v_permlane32_swap_b32_e32 v172, v174
	v_permlane32_swap_b32_e32 v173, v175
	s_nop 1
	v_permlane16_swap_b32_e32 v172, v174
	v_permlane16_swap_b32_e32 v173, v175
	global_store_dwordx4 v[222:223], v[172:175], off
	s_waitcnt vmcnt(4)
	v_fma_f32 v0, v36, v208, v0
	v_fma_f32 v1, v37, v209, v1
	v_fma_f32 v2, v38, v210, v2
	v_fma_f32 v3, v39, v211, v3
	v_fma_f32 v4, v32, v212, v4
	v_fma_f32 v5, v33, v213, v5
	v_fma_f32 v6, v34, v214, v6
	v_fma_f32 v7, v35, v215, v7
	v_cvt_pk_bf16_f32 v0, v0, v1
	v_cvt_pk_bf16_f32 v1, v2, v3
	v_cvt_pk_bf16_f32 v2, v4, v5
	v_cvt_pk_bf16_f32 v3, v6, v7
	s_mov_b32 s30, 0x160000
	s_mov_b32 s31, 0
	v_lshl_add_u64 v[222:223], v[218:219], 0, s[30:31]
	s_nop 1
	v_permlane32_swap_b32_e32 v0, v2
	v_permlane32_swap_b32_e32 v1, v3
	s_nop 1
	v_permlane16_swap_b32_e32 v0, v2
	v_permlane16_swap_b32_e32 v1, v3
	global_store_dwordx4 v[222:223], v[0:3], off offset:256
	s_cbranch_vccnz .Lp4pf_skip
	v_lshl_or_b32 v224, s20, 8, v197
	v_mov_b32_e32 v225, 0
	v_lshl_add_u32 v228, s22, 8, v180
	v_mov_b32_e32 v229, 0
	v_lshlrev_b64 v[216:217], 14, v[228:229]
	v_lshl_add_u64 v[216:217], v[216:217], 0, s[8:9]
	v_lshl_add_u64 v[216:217], v[224:225], 2, v[216:217]
	s_mov_b32 s30, 0x0
	s_mov_b32 s31, 0
	v_lshl_add_u64 v[220:221], v[216:217], 0, s[30:31]
	global_load_dword v232, v[220:221], off
	global_load_dword v232, v[220:221], off offset:512
	s_mov_b32 s30, 0x40000
	s_mov_b32 s31, 0
	v_lshl_add_u64 v[220:221], v[216:217], 0, s[30:31]
	global_load_dword v232, v[220:221], off
	global_load_dword v232, v[220:221], off offset:512
	s_mov_b32 s30, 0x80000
	s_mov_b32 s31, 0
	v_lshl_add_u64 v[220:221], v[216:217], 0, s[30:31]
	global_load_dword v232, v[220:221], off
	global_load_dword v232, v[220:221], off offset:512
	s_mov_b32 s30, 0xc0000
	s_mov_b32 s31, 0
	v_lshl_add_u64 v[220:221], v[216:217], 0, s[30:31]
	global_load_dword v232, v[220:221], off
	global_load_dword v232, v[220:221], off offset:512
	s_mov_b32 s30, 0x200000
	s_mov_b32 s31, 0
	v_lshl_add_u64 v[220:221], v[216:217], 0, s[30:31]
	global_load_dword v232, v[220:221], off
	global_load_dword v232, v[220:221], off offset:512
	s_mov_b32 s30, 0x240000
	s_mov_b32 s31, 0
	v_lshl_add_u64 v[220:221], v[216:217], 0, s[30:31]
	global_load_dword v232, v[220:221], off
	global_load_dword v232, v[220:221], off offset:512
	s_mov_b32 s30, 0x280000
	s_mov_b32 s31, 0
	v_lshl_add_u64 v[220:221], v[216:217], 0, s[30:31]
	global_load_dword v232, v[220:221], off
	global_load_dword v232, v[220:221], off offset:512
	s_mov_b32 s30, 0x2c0000
	s_mov_b32 s31, 0
	v_lshl_add_u64 v[220:221], v[216:217], 0, s[30:31]
	global_load_dword v232, v[220:221], off
	global_load_dword v232, v[220:221], off offset:512
.Lp4pf_skip:
	s_cbranch_vccnz .LBB0_554
	s_andn2_b64 vcc, exec, s[10:11]
	s_cbranch_vccnz .LBB0_553
	s_barrier
	s_branch .LBB0_553
